# combo11 + strategy 8 (MFMA shadow): in the P2/P4/P10 fp8 loops two of each load phase's four LDS-DMA pieces issue inside the following MFMA phase (after MFMA 4 and 12); waits vmcnt 8->6, 6->4
# baseline (speedup 1.0000x reference)
.LBB0_200:
	s_add_u32 s72, s42, 0xfff80000
	s_addc_u32 s73, s43, -1
	s_mov_b32 m0, s57
	s_nop 0
	global_load_lds_dwordx4 v160, s[72:73]
	s_mov_b32 m0, s58
	s_nop 0
	global_load_lds_dwordx4 v164, s[72:73]
	ds_read_b128 v[16:19], v186
	ds_read_b128 v[20:23], v187
	ds_read_b128 v[24:27], v188
	ds_read_b128 v[28:31], v189
	ds_read_b128 v[0:3], v190
	ds_read_b128 v[4:7], v191
	ds_read_b128 v[8:11], v192
	ds_read_b128 v[12:15], v193
	s_add_u32 s44, s42, 0xfff80080
	s_addc_u32 s45, s43, -1
	s_cmp_eq_u32 s68, 28
	s_cselect_b32 s47, s31, s45
	s_cselect_b32 s46, s35, s44
	s_cselect_b32 s45, s29, s67
	s_cselect_b32 s44, s39, s66
	ds_read_b128 v[178:181], v218
	ds_read_b128 v[182:185], v218 offset:1024
	ds_read_b128 v[222:225], v218 offset:2048
	ds_read_b128 v[226:229], v218 offset:3072
	ds_read_b128 v[230:233], v218 offset:4096
	ds_read_b128 v[234:237], v218 offset:5120
	ds_read_b128 v[238:241], v218 offset:6144
	ds_read_b128 v[242:245], v218 offset:7168
	s_waitcnt vmcnt(6)
	s_waitcnt lgkmcnt(0)
	s_barrier
	s_setprio 1
	s_waitcnt lgkmcnt(0)
	v_mfma_f32_16x16x128_f8f6f4 v[156:159], v[16:23], v[178:185], v[156:159]
	v_mfma_f32_16x16x128_f8f6f4 v[152:155], v[24:31], v[178:185], v[152:155]
	v_mfma_f32_16x16x128_f8f6f4 v[144:147], v[24:31], v[222:229], v[144:147]
	v_mfma_f32_16x16x128_f8f6f4 v[148:151], v[16:23], v[222:229], v[148:151]
	s_add_i32 m0, s27, 0xc000
	s_nop 0
	global_load_lds_dwordx4 v172, s[42:43]
	v_mfma_f32_16x16x128_f8f6f4 v[140:143], v[16:23], v[230:237], v[140:143]
	v_mfma_f32_16x16x128_f8f6f4 v[136:139], v[24:31], v[230:237], v[136:139]
	v_mfma_f32_16x16x128_f8f6f4 v[128:131], v[24:31], v[238:245], v[128:131]
	v_mfma_f32_16x16x128_f8f6f4 v[132:135], v[16:23], v[238:245], v[132:135]
	s_setprio 0
	s_setprio 1
	v_mfma_f32_16x16x128_f8f6f4 v[100:103], v[0:7], v[238:245], v[100:103]
	v_mfma_f32_16x16x128_f8f6f4 v[96:99], v[8:15], v[238:245], v[96:99]
	v_mfma_f32_16x16x128_f8f6f4 v[104:107], v[8:15], v[230:237], v[104:107]
	v_mfma_f32_16x16x128_f8f6f4 v[108:111], v[0:7], v[230:237], v[108:111]
	s_add_i32 m0, s27, 0xe000
	s_nop 0
	global_load_lds_dwordx4 v174, s[42:43]
	v_mfma_f32_16x16x128_f8f6f4 v[116:119], v[0:7], v[222:229], v[116:119]
	v_mfma_f32_16x16x128_f8f6f4 v[112:115], v[8:15], v[222:229], v[112:115]
	v_mfma_f32_16x16x128_f8f6f4 v[120:123], v[8:15], v[178:185], v[120:123]
	v_mfma_f32_16x16x128_f8f6f4 v[124:127], v[0:7], v[178:185], v[124:127]
	s_setprio 0
	s_barrier
	s_mov_b32 m0, s33
	v_lshl_add_u64 v[178:179], s[44:45], 0, v[162:163]
	s_add_u32 s70, s44, 0x80000
	ds_read_b128 v[222:225], v218 offset:16384
	ds_read_b128 v[226:229], v218 offset:17408
	ds_read_b128 v[230:233], v218 offset:18432
	ds_read_b128 v[234:237], v218 offset:19456
	ds_read_b128 v[238:241], v218 offset:20480
	ds_read_b128 v[242:245], v218 offset:21504
	ds_read_b128 v[246:249], v218 offset:22528
	ds_read_b128 v[250:253], v218 offset:23552
	global_load_lds_dwordx4 v[178:179], off
	v_lshl_add_u64 v[180:181], s[44:45], 0, v[166:167]
	s_mov_b32 m0, s48
	s_addc_u32 s71, s45, 0
	global_load_lds_dwordx4 v[180:181], off
	s_waitcnt vmcnt(4)
	s_waitcnt lgkmcnt(0)
	s_barrier
	s_setprio 1
	s_waitcnt lgkmcnt(0)
	v_mfma_f32_16x16x128_f8f6f4 v[92:95], v[16:23], v[222:229], v[92:95]
	v_mfma_f32_16x16x128_f8f6f4 v[88:91], v[24:31], v[222:229], v[88:91]
	v_mfma_f32_16x16x128_f8f6f4 v[80:83], v[24:31], v[230:237], v[80:83]
	v_mfma_f32_16x16x128_f8f6f4 v[84:87], v[16:23], v[230:237], v[84:87]
	s_mov_b32 m0, s49
	s_nop 0
	global_load_lds_dwordx4 v162, s[70:71]
	v_mfma_f32_16x16x128_f8f6f4 v[76:79], v[16:23], v[238:245], v[76:79]
	v_mfma_f32_16x16x128_f8f6f4 v[72:75], v[24:31], v[238:245], v[72:75]
	v_mfma_f32_16x16x128_f8f6f4 v[64:67], v[24:31], v[246:253], v[64:67]
	v_mfma_f32_16x16x128_f8f6f4 v[68:71], v[16:23], v[246:253], v[68:71]
	s_setprio 0
	s_setprio 1
	v_mfma_f32_16x16x128_f8f6f4 v[36:39], v[0:7], v[246:253], v[36:39]
	v_mfma_f32_16x16x128_f8f6f4 v[32:35], v[8:15], v[246:253], v[32:35]
	v_mfma_f32_16x16x128_f8f6f4 v[40:43], v[8:15], v[238:245], v[40:43]
	v_mfma_f32_16x16x128_f8f6f4 v[44:47], v[0:7], v[238:245], v[44:47]
	s_mov_b32 m0, s50
	s_nop 0
	global_load_lds_dwordx4 v166, s[70:71]
	v_mfma_f32_16x16x128_f8f6f4 v[52:55], v[0:7], v[230:237], v[52:55]
	v_mfma_f32_16x16x128_f8f6f4 v[48:51], v[8:15], v[230:237], v[48:51]
	v_mfma_f32_16x16x128_f8f6f4 v[56:59], v[8:15], v[222:229], v[56:59]
	v_mfma_f32_16x16x128_f8f6f4 v[60:63], v[0:7], v[222:229], v[60:63]
	s_setprio 0
	s_barrier
	s_mov_b32 m0, s27
	s_nop 0
	global_load_lds_dwordx4 v160, s[46:47]
	s_mov_b32 m0, s51
	s_nop 0
	global_load_lds_dwordx4 v164, s[46:47]
	ds_read_b128 v[0:3], v194
	ds_read_b128 v[4:7], v195
	ds_read_b128 v[8:11], v196
	ds_read_b128 v[12:15], v197
	ds_read_b128 v[16:19], v198
	ds_read_b128 v[20:23], v199
	ds_read_b128 v[24:27], v200
	ds_read_b128 v[28:31], v201
	s_add_u32 s46, s46, 0x80000
	s_addc_u32 s47, s47, 0
	ds_read_b128 v[222:225], v218 offset:32768
	ds_read_b128 v[226:229], v218 offset:33792
	ds_read_b128 v[230:233], v218 offset:34816
	ds_read_b128 v[234:237], v218 offset:35840
	ds_read_b128 v[238:241], v218 offset:36864
	ds_read_b128 v[242:245], v218 offset:37888
	ds_read_b128 v[246:249], v218 offset:38912
	ds_read_b128 v[250:253], v218 offset:39936
	s_waitcnt vmcnt(6)
	s_waitcnt lgkmcnt(0)
	s_barrier
	s_setprio 1
	s_waitcnt lgkmcnt(0)
	v_mfma_f32_16x16x128_f8f6f4 v[156:159], v[0:7], v[222:229], v[156:159]
	v_mfma_f32_16x16x128_f8f6f4 v[152:155], v[8:15], v[222:229], v[152:155]
	v_mfma_f32_16x16x128_f8f6f4 v[144:147], v[8:15], v[230:237], v[144:147]
	v_mfma_f32_16x16x128_f8f6f4 v[148:151], v[0:7], v[230:237], v[148:151]
	s_mov_b32 m0, s52
	s_nop 0
	global_load_lds_dwordx4 v160, s[46:47]
	v_mfma_f32_16x16x128_f8f6f4 v[140:143], v[0:7], v[238:245], v[140:143]
	v_mfma_f32_16x16x128_f8f6f4 v[136:139], v[8:15], v[238:245], v[136:139]
	v_mfma_f32_16x16x128_f8f6f4 v[128:131], v[8:15], v[246:253], v[128:131]
	v_mfma_f32_16x16x128_f8f6f4 v[132:135], v[0:7], v[246:253], v[132:135]
	s_setprio 0
	s_setprio 1
	v_mfma_f32_16x16x128_f8f6f4 v[100:103], v[16:23], v[246:253], v[100:103]
	v_mfma_f32_16x16x128_f8f6f4 v[96:99], v[24:31], v[246:253], v[96:99]
	v_mfma_f32_16x16x128_f8f6f4 v[104:107], v[24:31], v[238:245], v[104:107]
	v_mfma_f32_16x16x128_f8f6f4 v[108:111], v[16:23], v[238:245], v[108:111]
	s_mov_b32 m0, s53
	s_nop 0
	global_load_lds_dwordx4 v164, s[46:47]
	v_mfma_f32_16x16x128_f8f6f4 v[116:119], v[16:23], v[230:237], v[116:119]
	v_mfma_f32_16x16x128_f8f6f4 v[112:115], v[24:31], v[230:237], v[112:115]
	v_mfma_f32_16x16x128_f8f6f4 v[120:123], v[24:31], v[222:229], v[120:123]
	v_mfma_f32_16x16x128_f8f6f4 v[124:127], v[16:23], v[222:229], v[124:127]
	s_setprio 0
	s_barrier
	s_mov_b32 m0, s55
	v_lshl_add_u64 v[176:177], v[178:179], 0, s[20:21]
	s_add_u32 s44, s44, 0x80080
	ds_read_b128 v[222:225], v218 offset:49152
	ds_read_b128 v[226:229], v218 offset:50176
	ds_read_b128 v[230:233], v218 offset:51200
	ds_read_b128 v[234:237], v218 offset:52224
	ds_read_b128 v[238:241], v218 offset:53248
	ds_read_b128 v[242:245], v218 offset:54272
	ds_read_b128 v[246:249], v218 offset:55296
	ds_read_b128 v[250:253], v218 offset:56320
	global_load_lds_dwordx4 v[176:177], off
	v_lshl_add_u64 v[176:177], v[180:181], 0, s[20:21]
	s_mov_b32 m0, s56
	s_addc_u32 s45, s45, 0
	global_load_lds_dwordx4 v[176:177], off
	s_waitcnt vmcnt(4)
	s_waitcnt lgkmcnt(0)
	s_barrier
	s_setprio 1
	s_waitcnt lgkmcnt(0)
	v_mfma_f32_16x16x128_f8f6f4 v[92:95], v[0:7], v[222:229], v[92:95]
	v_mfma_f32_16x16x128_f8f6f4 v[88:91], v[8:15], v[222:229], v[88:91]
	v_mfma_f32_16x16x128_f8f6f4 v[80:83], v[8:15], v[230:237], v[80:83]
	v_mfma_f32_16x16x128_f8f6f4 v[84:87], v[0:7], v[230:237], v[84:87]
	s_mov_b32 m0, s59
	s_nop 0
	global_load_lds_dwordx4 v162, s[44:45]
	v_mfma_f32_16x16x128_f8f6f4 v[76:79], v[0:7], v[238:245], v[76:79]
	v_mfma_f32_16x16x128_f8f6f4 v[72:75], v[8:15], v[238:245], v[72:75]
	v_mfma_f32_16x16x128_f8f6f4 v[64:67], v[8:15], v[246:253], v[64:67]
	v_mfma_f32_16x16x128_f8f6f4 v[68:71], v[0:7], v[246:253], v[68:71]
	s_setprio 0
	s_setprio 1
	v_mfma_f32_16x16x128_f8f6f4 v[36:39], v[16:23], v[246:253], v[36:39]
	v_mfma_f32_16x16x128_f8f6f4 v[32:35], v[24:31], v[246:253], v[32:35]
	v_mfma_f32_16x16x128_f8f6f4 v[40:43], v[24:31], v[238:245], v[40:43]
	v_mfma_f32_16x16x128_f8f6f4 v[44:47], v[16:23], v[238:245], v[44:47]
	s_mov_b32 m0, s60
	s_nop 0
	global_load_lds_dwordx4 v166, s[44:45]
	v_mfma_f32_16x16x128_f8f6f4 v[52:55], v[16:23], v[230:237], v[52:55]
	v_mfma_f32_16x16x128_f8f6f4 v[48:51], v[24:31], v[230:237], v[48:51]
	v_mfma_f32_16x16x128_f8f6f4 v[56:59], v[24:31], v[222:229], v[56:59]
	v_mfma_f32_16x16x128_f8f6f4 v[60:63], v[16:23], v[222:229], v[60:63]
	s_setprio 0
	s_barrier
	s_add_i32 s68, s68, 2
	s_add_u32 s42, s42, 0x100
	s_addc_u32 s43, s43, 0
	s_add_u32 s66, s66, 0x100
	s_addc_u32 s67, s67, 0
	s_cmp_gt_u32 s68, 29
	s_cbranch_scc0 .LBB0_200
	s_nop 15
	s_nop 15
	s_and_b64 vcc, exec, s[22:23]
	s_cbranch_vccz .LBB0_203
	s_barrier

.LBB0_562:
	s_add_u32 s72, s30, 0xfff80000
	s_addc_u32 s73, s31, -1
	s_mov_b32 m0, s49
	s_nop 0
	global_load_lds_dwordx4 v160, s[72:73]
	s_mov_b32 m0, s50
	s_nop 0
	global_load_lds_dwordx4 v162, s[72:73]
	ds_read_b128 v[16:19], v181
	ds_read_b128 v[20:23], v182
	ds_read_b128 v[24:27], v183
	ds_read_b128 v[28:31], v184
	ds_read_b128 v[0:3], v185
	ds_read_b128 v[4:7], v186
	ds_read_b128 v[8:11], v187
	ds_read_b128 v[12:15], v188
	s_add_u32 s34, s30, 0xfff80080
	s_addc_u32 s35, s31, -1
	s_cmp_eq_u32 s59, 28
	s_cselect_b32 s37, s23, s35
	s_cselect_b32 s36, s55, s34
	s_cselect_b32 s35, s21, s58
	s_cselect_b32 s34, s56, s57
	ds_read_b128 v[172:175], v198
	ds_read_b128 v[176:179], v198 offset:1024
	ds_read_b128 v[200:203], v198 offset:2048
	ds_read_b128 v[204:207], v198 offset:3072
	ds_read_b128 v[208:211], v198 offset:4096
	ds_read_b128 v[212:215], v198 offset:5120
	ds_read_b128 v[216:219], v198 offset:6144
	ds_read_b128 v[220:223], v198 offset:7168
	s_waitcnt vmcnt(6)
	s_waitcnt lgkmcnt(0)
	s_barrier
	s_setprio 1
	s_waitcnt lgkmcnt(0)
	v_mfma_f32_16x16x128_f8f6f4 v[156:159], v[16:23], v[172:179], v[156:159]
	v_mfma_f32_16x16x128_f8f6f4 v[152:155], v[24:31], v[172:179], v[152:155]
	v_mfma_f32_16x16x128_f8f6f4 v[144:147], v[24:31], v[200:207], v[144:147]
	v_mfma_f32_16x16x128_f8f6f4 v[148:151], v[16:23], v[200:207], v[148:151]
	s_add_i32 m0, s29, 0xc000
	s_nop 0
	global_load_lds_dwordx4 v164, s[30:31]
	v_mfma_f32_16x16x128_f8f6f4 v[124:127], v[16:23], v[208:215], v[124:127]
	v_mfma_f32_16x16x128_f8f6f4 v[120:123], v[24:31], v[208:215], v[120:123]
	v_mfma_f32_16x16x128_f8f6f4 v[112:115], v[24:31], v[216:223], v[112:115]
	v_mfma_f32_16x16x128_f8f6f4 v[116:119], v[16:23], v[216:223], v[116:119]
	s_setprio 0
	s_setprio 1
	v_mfma_f32_16x16x128_f8f6f4 v[100:103], v[0:7], v[216:223], v[100:103]
	v_mfma_f32_16x16x128_f8f6f4 v[96:99], v[8:15], v[216:223], v[96:99]
	v_mfma_f32_16x16x128_f8f6f4 v[104:107], v[8:15], v[208:215], v[104:107]
	v_mfma_f32_16x16x128_f8f6f4 v[108:111], v[0:7], v[208:215], v[108:111]
	s_add_i32 m0, s29, 0xe000
	s_nop 0
	global_load_lds_dwordx4 v166, s[30:31]
	v_mfma_f32_16x16x128_f8f6f4 v[132:135], v[0:7], v[200:207], v[132:135]
	v_mfma_f32_16x16x128_f8f6f4 v[128:131], v[8:15], v[200:207], v[128:131]
	v_mfma_f32_16x16x128_f8f6f4 v[136:139], v[8:15], v[172:179], v[136:139]
	v_mfma_f32_16x16x128_f8f6f4 v[140:143], v[0:7], v[172:179], v[140:143]
	s_setprio 0
	s_barrier
	s_mov_b32 m0, s33
	v_lshl_add_u64 v[172:173], s[34:35], 0, v[160:161]
	s_add_u32 s60, s34, 0x80000
	ds_read_b128 v[200:203], v198 offset:16384
	ds_read_b128 v[204:207], v198 offset:17408
	ds_read_b128 v[208:211], v198 offset:18432
	ds_read_b128 v[212:215], v198 offset:19456
	ds_read_b128 v[216:219], v198 offset:20480
	ds_read_b128 v[220:223], v198 offset:21504
	ds_read_b128 v[224:227], v198 offset:22528
	ds_read_b128 v[228:231], v198 offset:23552
	global_load_lds_dwordx4 v[172:173], off
	v_lshl_add_u64 v[174:175], s[34:35], 0, v[162:163]
	s_mov_b32 m0, s38
	s_addc_u32 s61, s35, 0
	global_load_lds_dwordx4 v[174:175], off
	s_waitcnt vmcnt(4)
	s_waitcnt lgkmcnt(0)
	s_barrier
	s_setprio 1
	s_waitcnt lgkmcnt(0)
	v_mfma_f32_16x16x128_f8f6f4 v[92:95], v[16:23], v[200:207], v[92:95]
	v_mfma_f32_16x16x128_f8f6f4 v[88:91], v[24:31], v[200:207], v[88:91]
	v_mfma_f32_16x16x128_f8f6f4 v[80:83], v[24:31], v[208:215], v[80:83]
	v_mfma_f32_16x16x128_f8f6f4 v[84:87], v[16:23], v[208:215], v[84:87]
	s_mov_b32 m0, s39
	s_nop 0
	global_load_lds_dwordx4 v160, s[60:61]
	v_mfma_f32_16x16x128_f8f6f4 v[60:63], v[16:23], v[216:223], v[60:63]
	v_mfma_f32_16x16x128_f8f6f4 v[56:59], v[24:31], v[216:223], v[56:59]
	v_mfma_f32_16x16x128_f8f6f4 v[48:51], v[24:31], v[224:231], v[48:51]
	v_mfma_f32_16x16x128_f8f6f4 v[52:55], v[16:23], v[224:231], v[52:55]
	s_setprio 0
	s_setprio 1
	v_mfma_f32_16x16x128_f8f6f4 v[36:39], v[0:7], v[224:231], v[36:39]
	v_mfma_f32_16x16x128_f8f6f4 v[32:35], v[8:15], v[224:231], v[32:35]
	v_mfma_f32_16x16x128_f8f6f4 v[40:43], v[8:15], v[216:223], v[40:43]
	v_mfma_f32_16x16x128_f8f6f4 v[44:47], v[0:7], v[216:223], v[44:47]
	s_mov_b32 m0, s40
	s_nop 0
	global_load_lds_dwordx4 v162, s[60:61]
	v_mfma_f32_16x16x128_f8f6f4 v[68:71], v[0:7], v[208:215], v[68:71]
	v_mfma_f32_16x16x128_f8f6f4 v[64:67], v[8:15], v[208:215], v[64:67]
	v_mfma_f32_16x16x128_f8f6f4 v[72:75], v[8:15], v[200:207], v[72:75]
	v_mfma_f32_16x16x128_f8f6f4 v[76:79], v[0:7], v[200:207], v[76:79]
	s_setprio 0
	s_barrier
	s_mov_b32 m0, s29
	s_nop 0
	global_load_lds_dwordx4 v160, s[36:37]
	s_mov_b32 m0, s41
	s_nop 0
	global_load_lds_dwordx4 v162, s[36:37]
	ds_read_b128 v[0:3], v189
	ds_read_b128 v[4:7], v190
	ds_read_b128 v[8:11], v191
	ds_read_b128 v[12:15], v192
	ds_read_b128 v[16:19], v193
	ds_read_b128 v[20:23], v194
	ds_read_b128 v[24:27], v195
	ds_read_b128 v[28:31], v196
	s_add_u32 s36, s36, 0x80000
	s_addc_u32 s37, s37, 0
	ds_read_b128 v[200:203], v198 offset:32768
	ds_read_b128 v[204:207], v198 offset:33792
	ds_read_b128 v[208:211], v198 offset:34816
	ds_read_b128 v[212:215], v198 offset:35840
	ds_read_b128 v[216:219], v198 offset:36864
	ds_read_b128 v[220:223], v198 offset:37888
	ds_read_b128 v[224:227], v198 offset:38912
	ds_read_b128 v[228:231], v198 offset:39936
	s_waitcnt vmcnt(6)
	s_waitcnt lgkmcnt(0)
	s_barrier
	s_setprio 1
	s_waitcnt lgkmcnt(0)
	v_mfma_f32_16x16x128_f8f6f4 v[156:159], v[0:7], v[200:207], v[156:159]
	v_mfma_f32_16x16x128_f8f6f4 v[152:155], v[8:15], v[200:207], v[152:155]
	v_mfma_f32_16x16x128_f8f6f4 v[144:147], v[8:15], v[208:215], v[144:147]
	v_mfma_f32_16x16x128_f8f6f4 v[148:151], v[0:7], v[208:215], v[148:151]
	s_mov_b32 m0, s42
	s_nop 0
	global_load_lds_dwordx4 v160, s[36:37]
	v_mfma_f32_16x16x128_f8f6f4 v[124:127], v[0:7], v[216:223], v[124:127]
	v_mfma_f32_16x16x128_f8f6f4 v[120:123], v[8:15], v[216:223], v[120:123]
	v_mfma_f32_16x16x128_f8f6f4 v[112:115], v[8:15], v[224:231], v[112:115]
	v_mfma_f32_16x16x128_f8f6f4 v[116:119], v[0:7], v[224:231], v[116:119]
	s_setprio 0
	s_setprio 1
	v_mfma_f32_16x16x128_f8f6f4 v[100:103], v[16:23], v[224:231], v[100:103]
	v_mfma_f32_16x16x128_f8f6f4 v[96:99], v[24:31], v[224:231], v[96:99]
	v_mfma_f32_16x16x128_f8f6f4 v[104:107], v[24:31], v[216:223], v[104:107]
	v_mfma_f32_16x16x128_f8f6f4 v[108:111], v[16:23], v[216:223], v[108:111]
	s_mov_b32 m0, s43
	s_nop 0
	global_load_lds_dwordx4 v162, s[36:37]
	v_mfma_f32_16x16x128_f8f6f4 v[132:135], v[16:23], v[208:215], v[132:135]
	v_mfma_f32_16x16x128_f8f6f4 v[128:131], v[24:31], v[208:215], v[128:131]
	v_mfma_f32_16x16x128_f8f6f4 v[136:139], v[24:31], v[200:207], v[136:139]
	v_mfma_f32_16x16x128_f8f6f4 v[140:143], v[16:23], v[200:207], v[140:143]
	s_setprio 0
	s_barrier
	s_mov_b32 m0, s47
	v_lshl_add_u64 v[172:173], v[172:173], 0, s[14:15]
	s_add_u32 s34, s34, 0x80080
	ds_read_b128 v[200:203], v198 offset:49152
	ds_read_b128 v[204:207], v198 offset:50176
	ds_read_b128 v[208:211], v198 offset:51200
	ds_read_b128 v[212:215], v198 offset:52224
	ds_read_b128 v[216:219], v198 offset:53248
	ds_read_b128 v[220:223], v198 offset:54272
	ds_read_b128 v[224:227], v198 offset:55296
	ds_read_b128 v[228:231], v198 offset:56320
	global_load_lds_dwordx4 v[172:173], off
	v_lshl_add_u64 v[172:173], v[174:175], 0, s[14:15]
	s_mov_b32 m0, s48
	s_addc_u32 s35, s35, 0
	global_load_lds_dwordx4 v[172:173], off
	s_waitcnt vmcnt(4)
	s_waitcnt lgkmcnt(0)
	s_barrier
	s_setprio 1
	s_waitcnt lgkmcnt(0)
	v_mfma_f32_16x16x128_f8f6f4 v[92:95], v[0:7], v[200:207], v[92:95]
	v_mfma_f32_16x16x128_f8f6f4 v[88:91], v[8:15], v[200:207], v[88:91]
	v_mfma_f32_16x16x128_f8f6f4 v[80:83], v[8:15], v[208:215], v[80:83]
	v_mfma_f32_16x16x128_f8f6f4 v[84:87], v[0:7], v[208:215], v[84:87]
	s_mov_b32 m0, s51
	s_nop 0
	global_load_lds_dwordx4 v160, s[34:35]
	v_mfma_f32_16x16x128_f8f6f4 v[60:63], v[0:7], v[216:223], v[60:63]
	v_mfma_f32_16x16x128_f8f6f4 v[56:59], v[8:15], v[216:223], v[56:59]
	v_mfma_f32_16x16x128_f8f6f4 v[48:51], v[8:15], v[224:231], v[48:51]
	v_mfma_f32_16x16x128_f8f6f4 v[52:55], v[0:7], v[224:231], v[52:55]
	s_setprio 0
	s_setprio 1
	v_mfma_f32_16x16x128_f8f6f4 v[36:39], v[16:23], v[224:231], v[36:39]
	v_mfma_f32_16x16x128_f8f6f4 v[32:35], v[24:31], v[224:231], v[32:35]
	v_mfma_f32_16x16x128_f8f6f4 v[40:43], v[24:31], v[216:223], v[40:43]
	v_mfma_f32_16x16x128_f8f6f4 v[44:47], v[16:23], v[216:223], v[44:47]
	s_mov_b32 m0, s52
	s_nop 0
	global_load_lds_dwordx4 v162, s[34:35]
	v_mfma_f32_16x16x128_f8f6f4 v[68:71], v[16:23], v[208:215], v[68:71]
	v_mfma_f32_16x16x128_f8f6f4 v[64:67], v[24:31], v[208:215], v[64:67]
	v_mfma_f32_16x16x128_f8f6f4 v[72:75], v[24:31], v[200:207], v[72:75]
	v_mfma_f32_16x16x128_f8f6f4 v[76:79], v[16:23], v[200:207], v[76:79]
	s_setprio 0
	s_barrier
	s_add_i32 s59, s59, 2
	s_add_u32 s30, s30, 0x100
	s_addc_u32 s31, s31, 0
	s_add_u32 s57, s57, 0x100
	s_addc_u32 s58, s58, 0
	s_cmp_gt_u32 s59, 29
	s_cbranch_scc0 .LBB0_562
	s_nop 15
	s_nop 15
	s_and_b64 vcc, exec, s[16:17]
	s_cbranch_vccz .LBB0_565
	s_barrier

.LBB0_1358:
	s_add_u32 s30, s26, 0x1000
	s_addc_u32 s31, s27, 0
	s_mov_b32 m0, s49
	s_nop 0
	global_load_lds_dwordx4 v160, s[30:31]
	s_mov_b32 m0, s50
	s_nop 0
	global_load_lds_dwordx4 v164, s[30:31]
	ds_read_b128 v[16:19], v207
	ds_read_b128 v[20:23], v208
	ds_read_b128 v[24:27], v209
	ds_read_b128 v[28:31], v210
	ds_read_b128 v[0:3], v211
	ds_read_b128 v[4:7], v212
	ds_read_b128 v[8:11], v213
	ds_read_b128 v[12:15], v214
	s_add_u32 s28, s26, 0x10000
	s_addc_u32 s29, s27, 0
	s_cmpk_eq_i32 s59, 0x7c
	s_cselect_b32 s36, s55, s28
	s_cselect_b32 s37, s19, s29
	s_cselect_b32 s34, s56, s57
	s_cselect_b32 s35, s17, s58
	ds_read_b128 v[176:179], v224
	ds_read_b128 v[180:183], v224 offset:1024
	ds_read_b128 v[184:187], v224 offset:2048
	ds_read_b128 v[188:191], v224 offset:3072
	ds_read_b128 v[192:195], v224 offset:4096
	ds_read_b128 v[196:199], v224 offset:5120
	ds_read_b128 v[226:229], v224 offset:6144
	ds_read_b128 v[230:233], v224 offset:7168
	s_waitcnt vmcnt(6)
	s_waitcnt lgkmcnt(0)
	s_barrier
	s_setprio 1
	s_waitcnt lgkmcnt(0)
	v_mfma_f32_16x16x128_f8f6f4 v[156:159], v[16:23], v[176:183], v[156:159]
	v_mfma_f32_16x16x128_f8f6f4 v[152:155], v[24:31], v[176:183], v[152:155]
	v_mfma_f32_16x16x128_f8f6f4 v[136:139], v[24:31], v[184:191], v[136:139]
	v_mfma_f32_16x16x128_f8f6f4 v[144:147], v[16:23], v[184:191], v[144:147]
	s_add_i32 m0, s25, 0xc000
	s_nop 0
	global_load_lds_dwordx4 v168, s[26:27]
	v_mfma_f32_16x16x128_f8f6f4 v[124:127], v[16:23], v[192:199], v[124:127]
	v_mfma_f32_16x16x128_f8f6f4 v[120:123], v[24:31], v[192:199], v[120:123]
	v_mfma_f32_16x16x128_f8f6f4 v[104:107], v[24:31], v[226:233], v[104:107]
	v_mfma_f32_16x16x128_f8f6f4 v[112:115], v[16:23], v[226:233], v[112:115]
	s_setprio 0
	s_setprio 1
	v_mfma_f32_16x16x128_f8f6f4 v[100:103], v[0:7], v[226:233], v[100:103]
	v_mfma_f32_16x16x128_f8f6f4 v[96:99], v[8:15], v[226:233], v[96:99]
	v_mfma_f32_16x16x128_f8f6f4 v[108:111], v[8:15], v[192:199], v[108:111]
	v_mfma_f32_16x16x128_f8f6f4 v[116:119], v[0:7], v[192:199], v[116:119]
	s_add_i32 m0, s25, 0xe000
	s_nop 0
	global_load_lds_dwordx4 v170, s[26:27]
	v_mfma_f32_16x16x128_f8f6f4 v[132:135], v[0:7], v[184:191], v[132:135]
	v_mfma_f32_16x16x128_f8f6f4 v[128:131], v[8:15], v[184:191], v[128:131]
	v_mfma_f32_16x16x128_f8f6f4 v[140:143], v[8:15], v[176:183], v[140:143]
	v_mfma_f32_16x16x128_f8f6f4 v[148:151], v[0:7], v[176:183], v[148:151]
	s_setprio 0
	s_barrier
	s_mov_b32 m0, s33
	v_lshl_add_u64 v[176:177], s[34:35], 0, v[162:163]
	s_add_u32 s26, s34, 0x200000
	ds_read_b128 v[180:183], v224 offset:16384
	ds_read_b128 v[184:187], v224 offset:17408
	ds_read_b128 v[188:191], v224 offset:18432
	ds_read_b128 v[192:195], v224 offset:19456
	ds_read_b128 v[196:199], v224 offset:20480
	ds_read_b128 v[200:203], v224 offset:21504
	ds_read_b128 v[226:229], v224 offset:22528
	ds_read_b128 v[230:233], v224 offset:23552
	global_load_lds_dwordx4 v[176:177], off
	v_lshl_add_u64 v[178:179], s[34:35], 0, v[166:167]
	s_mov_b32 m0, s38
	s_addc_u32 s27, s35, 0
	global_load_lds_dwordx4 v[178:179], off
	s_waitcnt vmcnt(4)
	s_waitcnt lgkmcnt(0)
	s_barrier
	s_setprio 1
	s_waitcnt lgkmcnt(0)
	v_mfma_f32_16x16x128_f8f6f4 v[92:95], v[16:23], v[180:187], v[92:95]
	v_mfma_f32_16x16x128_f8f6f4 v[88:91], v[24:31], v[180:187], v[88:91]
	v_mfma_f32_16x16x128_f8f6f4 v[72:75], v[24:31], v[188:195], v[72:75]
	v_mfma_f32_16x16x128_f8f6f4 v[80:83], v[16:23], v[188:195], v[80:83]
	s_mov_b32 m0, s39
	s_nop 0
	global_load_lds_dwordx4 v162, s[26:27]
	v_mfma_f32_16x16x128_f8f6f4 v[64:67], v[16:23], v[196:203], v[64:67]
	v_mfma_f32_16x16x128_f8f6f4 v[56:59], v[24:31], v[196:203], v[56:59]
	v_mfma_f32_16x16x128_f8f6f4 v[40:43], v[24:31], v[226:233], v[40:43]
	v_mfma_f32_16x16x128_f8f6f4 v[48:51], v[16:23], v[226:233], v[48:51]
	s_setprio 0
	s_setprio 1
	v_mfma_f32_16x16x128_f8f6f4 v[36:39], v[0:7], v[226:233], v[36:39]
	v_mfma_f32_16x16x128_f8f6f4 v[32:35], v[8:15], v[226:233], v[32:35]
	v_mfma_f32_16x16x128_f8f6f4 v[44:47], v[8:15], v[196:203], v[44:47]
	v_mfma_f32_16x16x128_f8f6f4 v[52:55], v[0:7], v[196:203], v[52:55]
	s_mov_b32 m0, s40
	s_nop 0
	global_load_lds_dwordx4 v166, s[26:27]
	v_mfma_f32_16x16x128_f8f6f4 v[68:71], v[0:7], v[188:195], v[68:71]
	v_mfma_f32_16x16x128_f8f6f4 v[60:63], v[8:15], v[188:195], v[60:63]
	v_mfma_f32_16x16x128_f8f6f4 v[76:79], v[8:15], v[180:187], v[76:79]
	v_mfma_f32_16x16x128_f8f6f4 v[84:87], v[0:7], v[180:187], v[84:87]
	s_setprio 0
	s_barrier
	s_mov_b32 m0, s25
	s_nop 0
	global_load_lds_dwordx4 v160, s[36:37]
	s_mov_b32 m0, s41
	s_nop 0
	global_load_lds_dwordx4 v164, s[36:37]
	ds_read_b128 v[0:3], v215
	ds_read_b128 v[4:7], v216
	ds_read_b128 v[8:11], v217
	ds_read_b128 v[12:15], v218
	ds_read_b128 v[16:19], v219
	ds_read_b128 v[20:23], v220
	ds_read_b128 v[24:27], v221
	ds_read_b128 v[28:31], v222
	s_add_u32 s26, s36, 0x8000
	s_addc_u32 s27, s37, 0
	ds_read_b128 v[180:183], v224 offset:32768
	ds_read_b128 v[184:187], v224 offset:33792
	ds_read_b128 v[188:191], v224 offset:34816
	ds_read_b128 v[192:195], v224 offset:35840
	ds_read_b128 v[196:199], v224 offset:36864
	ds_read_b128 v[200:203], v224 offset:37888
	ds_read_b128 v[226:229], v224 offset:38912
	ds_read_b128 v[230:233], v224 offset:39936
	s_waitcnt vmcnt(6)
	s_waitcnt lgkmcnt(0)
	s_barrier
	s_setprio 1
	s_waitcnt lgkmcnt(0)
	v_mfma_f32_16x16x128_f8f6f4 v[156:159], v[0:7], v[180:187], v[156:159]
	v_mfma_f32_16x16x128_f8f6f4 v[152:155], v[8:15], v[180:187], v[152:155]
	v_mfma_f32_16x16x128_f8f6f4 v[136:139], v[8:15], v[188:195], v[136:139]
	v_mfma_f32_16x16x128_f8f6f4 v[144:147], v[0:7], v[188:195], v[144:147]
	s_mov_b32 m0, s42
	s_nop 0
	global_load_lds_dwordx4 v160, s[26:27]
	v_mfma_f32_16x16x128_f8f6f4 v[124:127], v[0:7], v[196:203], v[124:127]
	v_mfma_f32_16x16x128_f8f6f4 v[120:123], v[8:15], v[196:203], v[120:123]
	v_mfma_f32_16x16x128_f8f6f4 v[104:107], v[8:15], v[226:233], v[104:107]
	v_mfma_f32_16x16x128_f8f6f4 v[112:115], v[0:7], v[226:233], v[112:115]
	s_setprio 0
	s_setprio 1
	v_mfma_f32_16x16x128_f8f6f4 v[100:103], v[16:23], v[226:233], v[100:103]
	v_mfma_f32_16x16x128_f8f6f4 v[96:99], v[24:31], v[226:233], v[96:99]
	v_mfma_f32_16x16x128_f8f6f4 v[108:111], v[24:31], v[196:203], v[108:111]
	v_mfma_f32_16x16x128_f8f6f4 v[116:119], v[16:23], v[196:203], v[116:119]
	s_mov_b32 m0, s43
	s_nop 0
	global_load_lds_dwordx4 v164, s[26:27]
	v_mfma_f32_16x16x128_f8f6f4 v[132:135], v[16:23], v[188:195], v[132:135]
	v_mfma_f32_16x16x128_f8f6f4 v[128:131], v[24:31], v[188:195], v[128:131]
	v_mfma_f32_16x16x128_f8f6f4 v[140:143], v[24:31], v[180:187], v[140:143]
	v_mfma_f32_16x16x128_f8f6f4 v[148:151], v[16:23], v[180:187], v[148:151]
	s_setprio 0
	s_barrier
	s_mov_b32 m0, s47
	v_lshl_add_u64 v[176:177], v[176:177], 0, s[10:11]
	s_add_u32 s26, s34, 0x200080
	ds_read_b128 v[180:183], v224 offset:49152
	ds_read_b128 v[184:187], v224 offset:50176
	ds_read_b128 v[188:191], v224 offset:51200
	ds_read_b128 v[192:195], v224 offset:52224
	ds_read_b128 v[196:199], v224 offset:53248
	ds_read_b128 v[200:203], v224 offset:54272
	ds_read_b128 v[226:229], v224 offset:55296
	ds_read_b128 v[230:233], v224 offset:56320
	global_load_lds_dwordx4 v[176:177], off
	v_lshl_add_u64 v[176:177], v[178:179], 0, s[10:11]
	s_mov_b32 m0, s48
	s_addc_u32 s27, s35, 0
	global_load_lds_dwordx4 v[176:177], off
	s_waitcnt vmcnt(4)
	s_waitcnt lgkmcnt(0)
	s_barrier
	s_setprio 1
	s_waitcnt lgkmcnt(0)
	v_mfma_f32_16x16x128_f8f6f4 v[92:95], v[0:7], v[180:187], v[92:95]
	v_mfma_f32_16x16x128_f8f6f4 v[88:91], v[8:15], v[180:187], v[88:91]
	v_mfma_f32_16x16x128_f8f6f4 v[72:75], v[8:15], v[188:195], v[72:75]
	v_mfma_f32_16x16x128_f8f6f4 v[80:83], v[0:7], v[188:195], v[80:83]
	s_mov_b32 m0, s51
	s_nop 0
	global_load_lds_dwordx4 v162, s[26:27]
	v_mfma_f32_16x16x128_f8f6f4 v[64:67], v[0:7], v[196:203], v[64:67]
	v_mfma_f32_16x16x128_f8f6f4 v[56:59], v[8:15], v[196:203], v[56:59]
	v_mfma_f32_16x16x128_f8f6f4 v[40:43], v[8:15], v[226:233], v[40:43]
	v_mfma_f32_16x16x128_f8f6f4 v[48:51], v[0:7], v[226:233], v[48:51]
	s_setprio 0
	s_setprio 1
	v_mfma_f32_16x16x128_f8f6f4 v[36:39], v[16:23], v[226:233], v[36:39]
	v_mfma_f32_16x16x128_f8f6f4 v[32:35], v[24:31], v[226:233], v[32:35]
	v_mfma_f32_16x16x128_f8f6f4 v[44:47], v[24:31], v[196:203], v[44:47]
	v_mfma_f32_16x16x128_f8f6f4 v[52:55], v[16:23], v[196:203], v[52:55]
	s_mov_b32 m0, s52
	s_nop 0
	global_load_lds_dwordx4 v166, s[26:27]
	v_mfma_f32_16x16x128_f8f6f4 v[68:71], v[16:23], v[188:195], v[68:71]
	v_mfma_f32_16x16x128_f8f6f4 v[60:63], v[24:31], v[188:195], v[60:63]
	v_mfma_f32_16x16x128_f8f6f4 v[76:79], v[24:31], v[180:187], v[76:79]
	v_mfma_f32_16x16x128_f8f6f4 v[84:87], v[16:23], v[180:187], v[84:87]
	s_setprio 0
	s_barrier
	s_add_i32 s59, s59, 2
	s_add_u32 s57, s57, 0x100
	s_addc_u32 s58, s58, 0
	s_cmpk_gt_u32 s59, 0x7d
	s_mov_b64 s[26:27], s[28:29]
	s_cbranch_scc0 .LBB0_1358
	s_nop 15
	s_nop 15
	s_and_b64 vcc, exec, s[12:13]
	s_cbranch_vccz .LBB0_1361
	s_barrier
